# weight-conversion tile loops (8 copies): source pointers loaded once per call instead of per tile, removing the per-tile full vmcnt(0) drain that waited for the previous tile's stores
# speedup vs baseline: 1.0169x; 1.0007x over previous
; #define LAS __attribute__((address_space(3)))
; __device__ __forceinline__ void tr_slack(const Ctx& P, LAS unsigned char* lds, unsigned* tilectr, unsigned* cnt, unsigned target) {
;     const int tid = threadIdx.x, lane = tid & 63, wave = __builtin_amdgcn_readfirstlane(tid >> 6);
;     volatile LAS int* box = (volatile LAS int*)(lds + LDS_MISC + 2048);
;     int r = -1; unsigned pollv = 0u;
;     if (tid == 0) { int stop0 = 0; if (cnt) stop0 = (__hip_atomic_load(cnt, __ATOMIC_RELAXED, __HIP_MEMORY_SCOPE_AGENT) >= target) ? 1 : 0;
;         box[0] = stop0 ? -1 : (int)__hip_atomic_fetch_add(tilectr, 1u, __ATOMIC_RELAXED, __HIP_MEMORY_SCOPE_AGENT); box[1] = stop0; }
;     __syncthreads();
;     int idx = box[0], stop = box[1];
;     const int sw = lane & 7;
.LBB0_594:
	s_or_b64 exec, exec, s[6:7]
	s_add_i32 s9, 0, 0x20800
	v_mov_b32_e32 v2, s9
	s_add_i32 s38, 0, 0x20804
	s_waitcnt lgkmcnt(0)
	s_barrier
	ds_read_b32 v2, v2
	v_mov_b32_e32 v3, s38
	ds_read_b32 v3, v3
	s_movk_i32 s4, 0x29ff
	s_mov_b32 s19, 0
	s_waitcnt lgkmcnt(1)
	v_cmp_lt_u32_e32 vcc, s4, v2
	v_readfirstlane_b32 s26, v2
	s_waitcnt lgkmcnt(0)
	v_readfirstlane_b32 s28, v3
	s_cbranch_vccnz .LBB0_612
	s_lshr_b32 s6, s22, 6
	s_lshl_b32 s40, s6, 4
	s_add_u32 s41, s36, 0x152c0000
	v_xor_b32_e32 v4, v169, v0
	s_addc_u32 s42, s37, 0
	v_lshlrev_b32_e32 v4, 4, v4
	v_or_b32_e32 v6, 0x200, v0
	v_or_b32_e32 v8, 0x600, v0
	s_add_u32 s20, s36, 0x5cec0000
	v_and_b32_e32 v2, 63, v0
	v_bitop3_b32 v3, s6, v0, 7 bitop3:0x78
	v_and_b32_e32 v4, 0x70, v4
	v_lshrrev_b32_e32 v81, 3, v6
	v_or_b32_e32 v82, 0x80, v1
	v_lshrrev_b32_e32 v83, 3, v8
	s_addc_u32 s21, s37, 0
	v_lshlrev_b32_e32 v80, 2, v2
	v_mov_b32_e32 v75, 0
	v_lshl_add_u32 v2, v2, 9, 0
	v_lshlrev_b32_e32 v3, 4, v3
	v_add_u32_e32 v4, 0, v4
	v_lshlrev_b32_e32 v5, 7, v1
	v_lshlrev_b32_e32 v6, 7, v81
	v_lshlrev_b32_e32 v7, 7, v82
	v_lshlrev_b32_e32 v8, 7, v83
	s_add_u32 s43, s36, 0x72c0000
	v_cmp_ne_u32_e64 s[4:5], 0, v0
	v_and_b32_e32 v76, 0x70, v168
	v_mov_b32_e32 v77, v75
	s_addc_u32 s44, s37, 0
	v_mov_b32_e32 v95, -1
	s_mov_b32 s45, 0xc3e00000
	s_mov_b32 s46, 0x42fe0000
	s_mov_b32 s47, 0x4b3fff81
	s_mov_b32 s48, 0xc0c0400
	s_mov_b32 s49, 0x5040100
	v_add_u32_e32 v84, v4, v5
	v_add_u32_e32 v85, v4, v6
	v_add_u32_e32 v86, v4, v7
	v_add_u32_e32 v87, v4, v8
	s_movk_i32 s50, 0x2a00
	v_mov_b32_e32 v88, 0x100
	v_mov_b32_e32 v89, 0xf8
	v_mov_b32_e32 v90, 0x3800000
	v_mov_b32_e32 v91, 0x7000
	v_add_u32_e32 v92, v2, v3
	v_mov_b32_e32 v93, 0x43e00000
	v_mov_b32_e32 v94, 0x4b40007f
	v_mov_b32_e32 v96, 0
	v_mov_b64_e32 v[240:241], s[12:13]
	flat_load_dwordx2 v[242:243], v[240:241] offset:256
	flat_load_dwordx2 v[244:245], v[240:241] offset:248
	flat_load_dwordx2 v[240:241], v[240:241] offset:264
	s_waitcnt vmcnt(0) lgkmcnt(0)
	s_branch .LBB0_597

; __device__ __forceinline__ TD tr_get(const Ctx& P, int it, int lane, int wave) {
;     ...
;     if (r < TR_I8) { const int nn = (r % 448) * 256 + q4, k0 = (r / 448) * 128; const int e = nn / 14336, n = nn % 14336, j = n >> 8, half = (n >> 7) & 1, w = n & 127;
;         t.p = (half ? P.in[32] : P.in[31]) + (size_t)e * DM * DFFE + (size_t)(k0 + kw) * DFFE + j * 128 + w; t.ld = DFFE; t.fp8 = 2; t.cm = (const float*)(ws + WS_MCM) + nn;
;         t.dst = ws + WS_WM1 + (size_t)(nn - q4) * 2048 + k0; t.dpitch = 2048; return t; } r -= TR_I8;
;     { const int nn = (r % 64) * 256 + q4, k0 = (r / 64) * 128; const int e = nn >> 11, n = nn & 2047;
;         t.p = P.in[33] + (size_t)e * DFFE * DM + (size_t)(k0 + kw) * DM + n; t.ld = DM; t.wscale = W2S; t.fp8 = 1;
;         t.dst = ws + WS_WM2 + (size_t)(nn - q4) * DFFE + k0; t.dpitch = DFFE; return t; }
.LBB0_597:
	s_cmpk_gt_u32 s26, 0x1bff
	s_cselect_b64 s[6:7], -1, 0
	s_and_b64 vcc, exec, s[6:7]
	s_cbranch_vccz .LBB0_600
	v_mov_b64_e32 v[2:3], v[240:241]
	s_add_i32 s18, s26, 0xffffe400
	s_lshl_b32 s22, s18, 8
	s_lshl_b32 s18, s18, 1
	s_and_b32 s24, s18, 0x7fffff80
	s_bfe_u32 s18, s22, 0x3000b
	s_mul_i32 s18, s18, 0x3800000
	s_and_b32 s23, s22, 0x3f00
	s_and_b32 s22, s22, 0x700
	v_or_b32_e32 v4, s22, v80
	s_mul_i32 s25, s23, 0x1c00
	v_lshlrev_b32_e32 v74, 2, v4
	s_waitcnt lgkmcnt(0)
	v_lshl_add_u64 v[2:3], v[2:3], 0, s[18:19]
	s_add_i32 s18, s24, s40
	s_lshl_b64 s[22:23], s[18:19], 13
	s_add_u32 s18, s41, s25
	v_lshl_add_u64 v[2:3], v[2:3], 0, s[22:23]
	s_addc_u32 s22, s42, 0
	s_add_u32 s24, s18, s24
	v_lshl_add_u64 v[6:7], v[2:3], 0, v[74:75]
	s_addc_u32 s25, s22, 0
	s_cbranch_execz .LBB0_601
	v_mov_b64_e32 v[78:79], 0
	s_mov_b32 s51, 0x43000000
	s_mov_b64 s[22:23], 0x1c00
	s_mov_b64 s[26:27], 0x800
	s_branch .LBB0_602
.LBB0_600:
.LBB0_601:
	s_bfe_u32 s18, s26, 0xa0006
	s_mulk_i32 s18, 0x2493
	s_lshr_b32 s18, s18, 16
	s_mul_i32 s22, s18, 0x1c0
	s_sub_i32 s24, s26, s22
	s_and_b32 s22, s24, 0xffff
	v_lshl_or_b32 v4, s22, 8, v80
	v_mul_hi_u32_u24_e32 v2, 0x924925, v4
	v_lshrrev_b32_e32 v2, 5, v2
	v_mul_u32_u24_e32 v2, 0x3800, v2
	v_sub_u32_e32 v5, v4, v2
	v_and_b32_e32 v2, 0x80, v5
	v_cmp_eq_u32_e32 vcc, 0, v2
	s_bfe_u32 s25, s24, 0xd0003
	s_mulk_i32 s25, 0x2493
	v_cndmask_b32_e32 v74, v88, v89, vcc
	v_cndmask_b32_e32 v2, v242, v244, vcc
	v_cndmask_b32_e32 v3, v243, v245, vcc
	s_mov_b64 s[22:23], 0x800
	s_lshl_b32 s18, s18, 7
	s_lshr_b32 s26, s25, 16
	s_add_i32 s23, s40, s18
	s_lshl_b32 s24, s24, 19
	v_and_b32_e32 v6, 0x7c, v5
	v_lshlrev_b32_e32 v5, 1, v5
	s_add_u32 s24, s43, s24
	v_and_b32_e32 v74, 0x7e00, v5
	s_addc_u32 s25, s44, 0
	s_add_u32 s24, s24, s18
	s_mov_b32 s51, 1.0
	s_addc_u32 s25, s25, 0
	s_waitcnt lgkmcnt(0)
	v_mad_u64_u32 v[2:3], s[26:27], s26, v90, v[2:3]
	v_mad_u64_u32 v[2:3], s[26:27], s23, v91, v[2:3]
	v_lshl_add_u64 v[2:3], v[2:3], 0, v[74:75]
	v_lshlrev_b32_e32 v74, 2, v6
	v_lshl_add_u64 v[6:7], v[2:3], 0, v[74:75]
	v_lshlrev_b32_e32 v74, 2, v4
	v_lshl_add_u64 v[78:79], s[20:21], 0, v[74:75]
	s_mov_b64 s[26:27], 0x1c00

; #define LAS __attribute__((address_space(3)))
; __device__ __forceinline__ void tr_slack(const Ctx& P, LAS unsigned char* lds, unsigned* tilectr, unsigned* cnt, unsigned target) {
;     const int tid = threadIdx.x, lane = tid & 63, wave = __builtin_amdgcn_readfirstlane(tid >> 6);
;     volatile LAS int* box = (volatile LAS int*)(lds + LDS_MISC + 2048);
;     int r = -1; unsigned pollv = 0u;
;     if (tid == 0) { int stop0 = 0; if (cnt) stop0 = (__hip_atomic_load(cnt, __ATOMIC_RELAXED, __HIP_MEMORY_SCOPE_AGENT) >= target) ? 1 : 0;
;         box[0] = stop0 ? -1 : (int)__hip_atomic_fetch_add(tilectr, 1u, __ATOMIC_RELAXED, __HIP_MEMORY_SCOPE_AGENT); box[1] = stop0; }
;     __syncthreads();
;     int idx = box[0], stop = box[1];
;     const int sw = lane & 7;
.LBB0_1253:
	s_or_b64 exec, exec, s[6:7]
	s_add_i32 s9, 0, 0x20800
	v_mov_b32_e32 v2, s9
	s_add_i32 s38, 0, 0x20804
	s_waitcnt lgkmcnt(0)
	s_barrier
	ds_read_b32 v2, v2
	v_mov_b32_e32 v3, s38
	ds_read_b32 v3, v3
	s_movk_i32 s4, 0x29ff
	s_mov_b32 s19, 0
	s_waitcnt lgkmcnt(1)
	v_cmp_lt_u32_e32 vcc, s4, v2
	v_readfirstlane_b32 s26, v2
	s_waitcnt lgkmcnt(0)
	v_readfirstlane_b32 s28, v3
	s_cbranch_vccnz .LBB0_1271
	s_lshr_b32 s6, s22, 6
	s_lshl_b32 s40, s6, 4
	v_lshrrev_b32_e32 v4, 5, v0
	s_add_u32 s41, s36, 0x152c0000
	v_xor_b32_e32 v4, v4, v0
	s_addc_u32 s42, s37, 0
	v_lshlrev_b32_e32 v4, 4, v4
	v_or_b32_e32 v6, 0x200, v0
	v_or_b32_e32 v8, 0x600, v0
	s_add_u32 s20, s36, 0x5cec0000
	v_and_b32_e32 v2, 63, v0
	v_bitop3_b32 v3, s6, v0, 7 bitop3:0x78
	v_and_b32_e32 v4, 0x70, v4
	v_lshrrev_b32_e32 v81, 3, v6
	v_or_b32_e32 v82, 0x80, v1
	v_lshrrev_b32_e32 v83, 3, v8
	s_addc_u32 s21, s37, 0
	v_lshlrev_b32_e32 v80, 2, v2
	v_mov_b32_e32 v75, 0
	v_lshl_add_u32 v2, v2, 9, 0
	v_lshlrev_b32_e32 v3, 4, v3
	v_add_u32_e32 v4, 0, v4
	v_lshlrev_b32_e32 v5, 7, v1
	v_lshlrev_b32_e32 v6, 7, v81
	v_lshlrev_b32_e32 v7, 7, v82
	v_lshlrev_b32_e32 v8, 7, v83
	s_add_u32 s43, s36, 0x72c0000
	v_cmp_ne_u32_e64 s[4:5], 0, v0
	v_and_b32_e32 v76, 0x70, v184
	v_mov_b32_e32 v77, v75
	s_addc_u32 s44, s37, 0
	v_mov_b32_e32 v95, -1
	s_mov_b32 s45, 0xc3e00000
	s_mov_b32 s46, 0x42fe0000
	s_mov_b32 s47, 0x4b3fff81
	s_mov_b32 s48, 0xc0c0400
	s_mov_b32 s49, 0x5040100
	v_add_u32_e32 v84, v4, v5
	v_add_u32_e32 v85, v4, v6
	v_add_u32_e32 v86, v4, v7
	v_add_u32_e32 v87, v4, v8
	s_movk_i32 s50, 0x2a00
	v_mov_b32_e32 v88, 0x100
	v_mov_b32_e32 v89, 0xf8
	v_mov_b32_e32 v90, 0x3800000
	v_mov_b32_e32 v91, 0x7000
	v_add_u32_e32 v92, v2, v3
	v_mov_b32_e32 v93, 0x43e00000
	v_mov_b32_e32 v94, 0x4b40007f
	v_mov_b32_e32 v96, 0
	v_mov_b64_e32 v[240:241], s[12:13]
	flat_load_dwordx2 v[242:243], v[240:241] offset:256
	flat_load_dwordx2 v[244:245], v[240:241] offset:248
	flat_load_dwordx2 v[240:241], v[240:241] offset:264
	s_waitcnt vmcnt(0) lgkmcnt(0)
	s_branch .LBB0_1256

; #define LAS __attribute__((address_space(3)))
; __device__ __forceinline__ void tr_slack(const Ctx& P, LAS unsigned char* lds, unsigned* tilectr, unsigned* cnt, unsigned target) {
;     const int tid = threadIdx.x, lane = tid & 63, wave = __builtin_amdgcn_readfirstlane(tid >> 6);
;     volatile LAS int* box = (volatile LAS int*)(lds + LDS_MISC + 2048);
;     int r = -1; unsigned pollv = 0u;
;     if (tid == 0) { int stop0 = 0; if (cnt) stop0 = (__hip_atomic_load(cnt, __ATOMIC_RELAXED, __HIP_MEMORY_SCOPE_AGENT) >= target) ? 1 : 0;
;         box[0] = stop0 ? -1 : (int)__hip_atomic_fetch_add(tilectr, 1u, __ATOMIC_RELAXED, __HIP_MEMORY_SCOPE_AGENT); box[1] = stop0; }
;     __syncthreads();
;     int idx = box[0], stop = box[1];
;     const int sw = lane & 7;
.LBB0_1433:
	s_or_b64 exec, exec, s[6:7]
	s_add_i32 s9, 0, 0x20800
	v_mov_b32_e32 v2, s9
	s_add_i32 s38, 0, 0x20804
	s_waitcnt lgkmcnt(0)
	s_barrier
	ds_read_b32 v2, v2
	v_mov_b32_e32 v3, s38
	ds_read_b32 v3, v3
	s_movk_i32 s4, 0x29ff
	s_mov_b32 s19, 0
	s_waitcnt lgkmcnt(1)
	v_cmp_lt_u32_e32 vcc, s4, v2
	v_readfirstlane_b32 s26, v2
	s_waitcnt lgkmcnt(0)
	v_readfirstlane_b32 s28, v3
	s_cbranch_vccnz .LBB0_1451
	s_lshr_b32 s6, s22, 6
	s_lshl_b32 s40, s6, 4
	s_add_u32 s41, s36, 0x152c0000
	v_xor_b32_e32 v4, v165, v0
	s_addc_u32 s42, s37, 0
	v_lshlrev_b32_e32 v4, 4, v4
	v_or_b32_e32 v6, 0x200, v0
	v_or_b32_e32 v8, 0x600, v0
	s_add_u32 s20, s36, 0x5cec0000
	v_and_b32_e32 v2, 63, v0
	v_bitop3_b32 v3, s6, v0, 7 bitop3:0x78
	v_and_b32_e32 v4, 0x70, v4
	v_lshrrev_b32_e32 v81, 3, v6
	v_or_b32_e32 v82, 0x80, v1
	v_lshrrev_b32_e32 v83, 3, v8
	s_addc_u32 s21, s37, 0
	v_lshlrev_b32_e32 v80, 2, v2
	v_mov_b32_e32 v75, 0
	v_lshl_add_u32 v2, v2, 9, 0
	v_lshlrev_b32_e32 v3, 4, v3
	v_add_u32_e32 v4, 0, v4
	v_lshlrev_b32_e32 v5, 7, v1
	v_lshlrev_b32_e32 v6, 7, v81
	v_lshlrev_b32_e32 v7, 7, v82
	v_lshlrev_b32_e32 v8, 7, v83
	s_add_u32 s43, s36, 0x72c0000
	v_cmp_ne_u32_e64 s[4:5], 0, v0
	v_and_b32_e32 v76, 0x70, v164
	v_mov_b32_e32 v77, v75
	s_addc_u32 s44, s37, 0
	v_mov_b32_e32 v95, -1
	s_mov_b32 s45, 0xc3e00000
	s_mov_b32 s46, 0x42fe0000
	s_mov_b32 s47, 0x4b3fff81
	s_mov_b32 s48, 0xc0c0400
	s_mov_b32 s49, 0x5040100
	v_add_u32_e32 v84, v4, v5
	v_add_u32_e32 v85, v4, v6
	v_add_u32_e32 v86, v4, v7
	v_add_u32_e32 v87, v4, v8
	s_movk_i32 s50, 0x2a00
	v_mov_b32_e32 v88, 0x100
	v_mov_b32_e32 v89, 0xf8
	v_mov_b32_e32 v90, 0x3800000
	v_mov_b32_e32 v91, 0x7000
	v_add_u32_e32 v92, v2, v3
	v_mov_b32_e32 v93, 0x43e00000
	v_mov_b32_e32 v94, 0x4b40007f
	v_mov_b32_e32 v96, 0
	v_mov_b64_e32 v[240:241], s[12:13]
	flat_load_dwordx2 v[242:243], v[240:241] offset:256
	flat_load_dwordx2 v[244:245], v[240:241] offset:248
	flat_load_dwordx2 v[240:241], v[240:241] offset:264
	s_waitcnt vmcnt(0) lgkmcnt(0)
	s_branch .LBB0_1436

; #define LAS __attribute__((address_space(3)))
; __device__ __forceinline__ void tr_slack(const Ctx& P, LAS unsigned char* lds, unsigned* tilectr, unsigned* cnt, unsigned target) {
;     const int tid = threadIdx.x, lane = tid & 63, wave = __builtin_amdgcn_readfirstlane(tid >> 6);
;     volatile LAS int* box = (volatile LAS int*)(lds + LDS_MISC + 2048);
;     int r = -1; unsigned pollv = 0u;
;     if (tid == 0) { int stop0 = 0; if (cnt) stop0 = (__hip_atomic_load(cnt, __ATOMIC_RELAXED, __HIP_MEMORY_SCOPE_AGENT) >= target) ? 1 : 0;
;         box[0] = stop0 ? -1 : (int)__hip_atomic_fetch_add(tilectr, 1u, __ATOMIC_RELAXED, __HIP_MEMORY_SCOPE_AGENT); box[1] = stop0; }
;     __syncthreads();
;     int idx = box[0], stop = box[1];
;     const int sw = lane & 7;
.LBB0_1583:
	s_or_b64 exec, exec, s[6:7]
	s_add_i32 s9, 0, 0x20800
	v_mov_b32_e32 v2, s9
	s_add_i32 s38, 0, 0x20804
	s_waitcnt lgkmcnt(0)
	s_barrier
	ds_read_b32 v2, v2
	v_mov_b32_e32 v3, s38
	ds_read_b32 v3, v3
	s_movk_i32 s4, 0x29ff
	s_mov_b32 s19, 0
	s_waitcnt lgkmcnt(1)
	v_cmp_lt_u32_e32 vcc, s4, v2
	v_readfirstlane_b32 s26, v2
	s_waitcnt lgkmcnt(0)
	v_readfirstlane_b32 s28, v3
	s_cbranch_vccnz .LBB0_1601
	s_lshr_b32 s6, s22, 6
	s_lshl_b32 s40, s6, 4
	v_lshrrev_b32_e32 v4, 5, v0
	s_add_u32 s41, s36, 0x152c0000
	v_xor_b32_e32 v4, v4, v0
	s_addc_u32 s42, s37, 0
	v_lshlrev_b32_e32 v4, 4, v4
	v_or_b32_e32 v6, 0x200, v0
	v_or_b32_e32 v8, 0x600, v0
	s_add_u32 s20, s36, 0x5cec0000
	v_and_b32_e32 v2, 63, v0
	v_bitop3_b32 v3, s6, v0, 7 bitop3:0x78
	v_and_b32_e32 v4, 0x70, v4
	v_lshrrev_b32_e32 v81, 3, v6
	v_or_b32_e32 v82, 0x80, v1
	v_lshrrev_b32_e32 v83, 3, v8
	s_addc_u32 s21, s37, 0
	v_lshlrev_b32_e32 v80, 2, v2
	v_mov_b32_e32 v75, 0
	v_lshl_add_u32 v2, v2, 9, 0
	v_lshlrev_b32_e32 v3, 4, v3
	v_add_u32_e32 v4, 0, v4
	v_lshlrev_b32_e32 v5, 7, v1
	v_lshlrev_b32_e32 v6, 7, v81
	v_lshlrev_b32_e32 v7, 7, v82
	v_lshlrev_b32_e32 v8, 7, v83
	s_add_u32 s43, s36, 0x72c0000
	v_cmp_ne_u32_e64 s[4:5], 0, v0
	v_and_b32_e32 v76, 0x70, v212
	v_mov_b32_e32 v77, v75
	s_addc_u32 s44, s37, 0
	v_mov_b32_e32 v95, -1
	s_mov_b32 s45, 0xc3e00000
	s_mov_b32 s46, 0x42fe0000
	s_mov_b32 s47, 0x4b3fff81
	s_mov_b32 s48, 0xc0c0400
	s_mov_b32 s49, 0x5040100
	v_add_u32_e32 v84, v4, v5
	v_add_u32_e32 v85, v4, v6
	v_add_u32_e32 v86, v4, v7
	v_add_u32_e32 v87, v4, v8
	s_movk_i32 s50, 0x2a00
	v_mov_b32_e32 v88, 0x100
	v_mov_b32_e32 v89, 0xf8
	v_mov_b32_e32 v90, 0x3800000
	v_mov_b32_e32 v91, 0x7000
	v_add_u32_e32 v92, v2, v3
	v_mov_b32_e32 v93, 0x43e00000
	v_mov_b32_e32 v94, 0x4b40007f
	v_mov_b32_e32 v96, 0
	v_mov_b64_e32 v[240:241], s[12:13]
	flat_load_dwordx2 v[242:243], v[240:241] offset:256
	flat_load_dwordx2 v[244:245], v[240:241] offset:248
	flat_load_dwordx2 v[240:241], v[240:241] offset:264
	s_waitcnt vmcnt(0) lgkmcnt(0)
	s_branch .LBB0_1586

; #define LAS __attribute__((address_space(3)))
; __device__ __forceinline__ void tr_slack(const Ctx& P, LAS unsigned char* lds, unsigned* tilectr, unsigned* cnt, unsigned target) {
;     const int tid = threadIdx.x, lane = tid & 63, wave = __builtin_amdgcn_readfirstlane(tid >> 6);
;     volatile LAS int* box = (volatile LAS int*)(lds + LDS_MISC + 2048);
;     int r = -1; unsigned pollv = 0u;
;     if (tid == 0) { int stop0 = 0; if (cnt) stop0 = (__hip_atomic_load(cnt, __ATOMIC_RELAXED, __HIP_MEMORY_SCOPE_AGENT) >= target) ? 1 : 0;
;         box[0] = stop0 ? -1 : (int)__hip_atomic_fetch_add(tilectr, 1u, __ATOMIC_RELAXED, __HIP_MEMORY_SCOPE_AGENT); box[1] = stop0; }
;     __syncthreads();
;     int idx = box[0], stop = box[1];
;     const int sw = lane & 7;
.LBB0_2075:
	s_or_b64 exec, exec, s[6:7]
	s_add_i32 s9, 0, 0x20800
	v_mov_b32_e32 v2, s9
	s_add_i32 s38, 0, 0x20804
	s_waitcnt lgkmcnt(0)
	s_barrier
	ds_read_b32 v2, v2
	v_mov_b32_e32 v3, s38
	ds_read_b32 v3, v3
	s_movk_i32 s4, 0x29ff
	s_mov_b32 s19, 0
	s_waitcnt lgkmcnt(1)
	v_cmp_lt_u32_e32 vcc, s4, v2
	v_readfirstlane_b32 s26, v2
	s_waitcnt lgkmcnt(0)
	v_readfirstlane_b32 s28, v3
	s_cbranch_vccnz .LBB0_2093
	s_lshr_b32 s6, s22, 6
	s_lshl_b32 s40, s6, 4
	s_add_u32 s41, s36, 0x152c0000
	v_xor_b32_e32 v4, v171, v0
	s_addc_u32 s42, s37, 0
	v_lshlrev_b32_e32 v4, 4, v4
	v_or_b32_e32 v6, 0x200, v0
	v_or_b32_e32 v8, 0x600, v0
	s_add_u32 s20, s36, 0x5cec0000
	v_and_b32_e32 v2, 63, v0
	v_bitop3_b32 v3, s6, v0, 7 bitop3:0x78
	v_and_b32_e32 v4, 0x70, v4
	v_lshrrev_b32_e32 v81, 3, v6
	v_or_b32_e32 v82, 0x80, v1
	v_lshrrev_b32_e32 v83, 3, v8
	s_addc_u32 s21, s37, 0
	v_lshlrev_b32_e32 v80, 2, v2
	v_mov_b32_e32 v75, 0
	v_lshl_add_u32 v2, v2, 9, 0
	v_lshlrev_b32_e32 v3, 4, v3
	v_add_u32_e32 v4, 0, v4
	v_lshlrev_b32_e32 v5, 7, v1
	v_lshlrev_b32_e32 v6, 7, v81
	v_lshlrev_b32_e32 v7, 7, v82
	v_lshlrev_b32_e32 v8, 7, v83
	s_add_u32 s43, s36, 0x72c0000
	v_cmp_ne_u32_e64 s[4:5], 0, v0
	v_and_b32_e32 v76, 0x70, v170
	v_mov_b32_e32 v77, v75
	s_addc_u32 s44, s37, 0
	v_mov_b32_e32 v95, -1
	s_mov_b32 s45, 0xc3e00000
	s_mov_b32 s46, 0x42fe0000
	s_mov_b32 s47, 0x4b3fff81
	s_mov_b32 s48, 0xc0c0400
	s_mov_b32 s49, 0x5040100
	v_add_u32_e32 v84, v4, v5
	v_add_u32_e32 v85, v4, v6
	v_add_u32_e32 v86, v4, v7
	v_add_u32_e32 v87, v4, v8
	s_movk_i32 s50, 0x2a00
	v_mov_b32_e32 v88, 0x100
	v_mov_b32_e32 v89, 0xf8
	v_mov_b32_e32 v90, 0x3800000
	v_mov_b32_e32 v91, 0x7000
	v_add_u32_e32 v92, v2, v3
	v_mov_b32_e32 v93, 0x43e00000
	v_mov_b32_e32 v94, 0x4b40007f
	v_mov_b32_e32 v96, 0
	v_mov_b64_e32 v[240:241], s[12:13]
	flat_load_dwordx2 v[242:243], v[240:241] offset:256
	flat_load_dwordx2 v[244:245], v[240:241] offset:248
	flat_load_dwordx2 v[240:241], v[240:241] offset:264
	s_waitcnt vmcnt(0) lgkmcnt(0)
	s_branch .LBB0_2078

; #define LAS __attribute__((address_space(3)))
; __device__ __forceinline__ void tr_slack(const Ctx& P, LAS unsigned char* lds, unsigned* tilectr, unsigned* cnt, unsigned target) {
;     const int tid = threadIdx.x, lane = tid & 63, wave = __builtin_amdgcn_readfirstlane(tid >> 6);
;     volatile LAS int* box = (volatile LAS int*)(lds + LDS_MISC + 2048);
;     int r = -1; unsigned pollv = 0u;
;     if (tid == 0) { int stop0 = 0; if (cnt) stop0 = (__hip_atomic_load(cnt, __ATOMIC_RELAXED, __HIP_MEMORY_SCOPE_AGENT) >= target) ? 1 : 0;
;         box[0] = stop0 ? -1 : (int)__hip_atomic_fetch_add(tilectr, 1u, __ATOMIC_RELAXED, __HIP_MEMORY_SCOPE_AGENT); box[1] = stop0; }
;     __syncthreads();
;     int idx = box[0], stop = box[1];
;     const int sw = lane & 7;
.LBB0_2381:
	s_or_b64 exec, exec, s[4:5]
	s_add_i32 s9, 0, 0x20800
	v_mov_b32_e32 v2, s9
	s_waitcnt lgkmcnt(0)
	s_barrier
	ds_read_b32 v2, v2
	s_add_i32 s34, 0, 0x20804
	v_mov_b32_e32 v3, s34
	ds_read_b32 v66, v3
	s_movk_i32 s4, 0x29ff
	s_waitcnt lgkmcnt(1)
	v_cmp_lt_u32_e32 vcc, s4, v2
	s_mov_b32 s15, 0
	v_readfirstlane_b32 s18, v2
	s_cbranch_vccnz .LBB0_2399
	s_lshr_b32 s6, s14, 6
	v_lshl_add_u32 v2, v1, 9, 0
	v_bitop3_b32 v1, s6, v0, 7 bitop3:0x78
	v_lshlrev_b32_e32 v3, 4, v1
	v_lshrrev_b32_e32 v1, 5, v0
	v_xor_b32_e32 v1, v1, v0
	s_lshl_b32 s35, s6, 4
	v_lshlrev_b32_e32 v1, 4, v1
	v_and_b32_e32 v1, 0x70, v1
	s_add_u32 s38, s36, 0x152c0000
	v_add_u32_e32 v4, 0, v1
	v_lshlrev_b32_e32 v1, 4, v0
	s_addc_u32 s40, s37, 0
	v_and_b32_e32 v76, 0x70, v1
	v_lshrrev_b32_e32 v1, 3, v0
	v_or_b32_e32 v6, 0x200, v0
	v_or_b32_e32 v8, 0x600, v0
	s_add_u32 s16, s36, 0x5cec0000
	v_lshrrev_b32_e32 v75, 3, v6
	v_or_b32_e32 v82, 0x80, v1
	v_lshrrev_b32_e32 v83, 3, v8
	s_addc_u32 s17, s37, 0
	v_mov_b32_e32 v79, 0
	v_lshlrev_b32_e32 v5, 7, v1
	v_lshlrev_b32_e32 v6, 7, v75
	v_lshlrev_b32_e32 v7, 7, v82
	v_lshlrev_b32_e32 v8, 7, v83
	s_add_u32 s41, s36, 0x72c0000
	v_cmp_ne_u32_e64 s[4:5], 0, v0
	v_mov_b32_e32 v77, v79
	s_addc_u32 s42, s37, 0
	v_mov_b32_e32 v95, -1
	s_mov_b32 s43, 0xc3e00000
	s_mov_b32 s44, 0x42fe0000
	s_mov_b32 s45, 0x4b3fff81
	s_mov_b32 s46, 0xc0c0400
	s_mov_b32 s47, 0x5040100
	v_add_u32_e32 v84, v4, v5
	v_add_u32_e32 v85, v4, v6
	v_add_u32_e32 v86, v4, v7
	v_add_u32_e32 v87, v4, v8
	s_movk_i32 s48, 0x2a00
	v_mov_b32_e32 v88, 0x100
	v_mov_b32_e32 v89, 0xf8
	v_mov_b32_e32 v90, 0x3800000
	v_mov_b32_e32 v91, 0x7000
	v_add_u32_e32 v92, v2, v3
	v_mov_b32_e32 v93, 0x43e00000
	v_mov_b32_e32 v94, 0x4b40007f
	v_mov_b64_e32 v[240:241], s[28:29]
	flat_load_dwordx2 v[242:243], v[240:241] offset:256
	flat_load_dwordx2 v[244:245], v[240:241] offset:248
	flat_load_dwordx2 v[240:241], v[240:241] offset:264
	s_waitcnt vmcnt(0) lgkmcnt(0)
	s_branch .LBB0_2384

; __device__ __forceinline__ TD tr_get(const Ctx& P, int it, int lane, int wave) {
;     ...
;     if (r < TR_I8) { const int nn = (r % 448) * 256 + q4, k0 = (r / 448) * 128; const int e = nn / 14336, n = nn % 14336, j = n >> 8, half = (n >> 7) & 1, w = n & 127;
;         t.p = (half ? P.in[32] : P.in[31]) + (size_t)e * DM * DFFE + (size_t)(k0 + kw) * DFFE + j * 128 + w; t.ld = DFFE; t.fp8 = 2; t.cm = (const float*)(ws + WS_MCM) + nn;
;         t.dst = ws + WS_WM1 + (size_t)(nn - q4) * 2048 + k0; t.dpitch = 2048; return t; } r -= TR_I8;
;     { const int nn = (r % 64) * 256 + q4, k0 = (r / 64) * 128; const int e = nn >> 11, n = nn & 2047;
;         t.p = P.in[33] + (size_t)e * DFFE * DM + (size_t)(k0 + kw) * DM + n; t.ld = DM; t.wscale = W2S; t.fp8 = 1;
;         t.dst = ws + WS_WM2 + (size_t)(nn - q4) * DFFE + k0; t.dpitch = DFFE; return t; }
.LBB0_2384:
	s_cmpk_gt_u32 s18, 0x1bff
	s_cselect_b64 s[10:11], -1, 0
	s_and_b64 vcc, exec, s[10:11]
	s_cbranch_vccz .LBB0_2387
	v_mov_b64_e32 v[2:3], v[240:241]
	s_add_i32 s6, s18, 0xffffe400
	s_lshl_b32 s7, s6, 8
	s_lshl_b32 s6, s6, 1
	s_and_b32 s20, s6, 0x7fffff80
	s_bfe_u32 s6, s7, 0x3000b
	s_mul_i32 s14, s6, 0x3800000
	s_and_b32 s19, s7, 0x3f00
	s_and_b32 s7, s7, 0x700
	v_or_b32_e32 v4, s7, v74
	s_mulk_i32 s19, 0x1c00
	v_lshlrev_b32_e32 v78, 2, v4
	s_waitcnt lgkmcnt(0)
	v_lshl_add_u64 v[2:3], v[2:3], 0, s[14:15]
	s_add_i32 s14, s20, s35
	s_lshl_b64 s[6:7], s[14:15], 13
	v_lshl_add_u64 v[2:3], v[2:3], 0, s[6:7]
	s_add_u32 s6, s38, s19
	s_addc_u32 s7, s40, 0
	s_add_u32 s20, s6, s20
	v_lshl_add_u64 v[6:7], v[2:3], 0, v[78:79]
	s_addc_u32 s21, s7, 0
	s_cbranch_execz .LBB0_2388
	v_mov_b64_e32 v[80:81], 0
	s_mov_b32 s49, 0x43000000
	s_mov_b64 s[18:19], 0x1c00
	s_mov_b64 s[6:7], 0x800
	s_branch .LBB0_2389
.LBB0_2387:
.LBB0_2388:
	s_bfe_u32 s6, s18, 0xa0006
	s_mulk_i32 s6, 0x2493
	s_lshr_b32 s6, s6, 16
	s_mul_i32 s7, s6, 0x1c0
	s_sub_i32 s7, s18, s7
	s_and_b32 s14, s7, 0xffff
	v_lshl_or_b32 v4, s14, 8, v74
	v_mul_hi_u32_u24_e32 v2, 0x924925, v4
	v_lshrrev_b32_e32 v2, 5, v2
	v_mul_u32_u24_e32 v2, 0x3800, v2
	v_sub_u32_e32 v5, v4, v2
	v_and_b32_e32 v2, 0x80, v5
	v_cmp_eq_u32_e32 vcc, 0, v2
	s_mov_b64 s[18:19], 0x800
	s_bfe_u32 s19, s7, 0xd0003
	v_cndmask_b32_e32 v78, v88, v89, vcc
	v_cndmask_b32_e32 v2, v242, v244, vcc
	v_cndmask_b32_e32 v3, v243, v245, vcc
	s_lshl_b32 s6, s6, 7
	s_mulk_i32 s19, 0x2493
	s_add_i32 s14, s35, s6
	s_lshl_b32 s7, s7, 19
	s_lshr_b32 s19, s19, 16
	s_add_u32 s7, s41, s7
	s_addc_u32 s21, s42, 0
	s_add_u32 s20, s7, s6
	v_and_b32_e32 v6, 0x7c, v5
	v_lshlrev_b32_e32 v5, 1, v5
	v_and_b32_e32 v78, 0x7e00, v5
	s_mov_b32 s49, 1.0
	s_addc_u32 s21, s21, 0
	s_waitcnt lgkmcnt(0)
	v_mad_u64_u32 v[2:3], s[6:7], s19, v90, v[2:3]
	v_mad_u64_u32 v[2:3], s[6:7], s14, v91, v[2:3]
	v_lshl_add_u64 v[2:3], v[2:3], 0, v[78:79]
	v_lshlrev_b32_e32 v78, 2, v6
	v_lshl_add_u64 v[6:7], v[2:3], 0, v[78:79]
	v_lshlrev_b32_e32 v78, 2, v4
	v_lshl_add_u64 v[80:81], s[16:17], 0, v[78:79]
	s_mov_b64 s[6:7], 0x1c00

; #define LAS __attribute__((address_space(3)))
; __device__ __forceinline__ void tr_slack(const Ctx& P, LAS unsigned char* lds, unsigned* tilectr, unsigned* cnt, unsigned target) {
;     const int tid = threadIdx.x, lane = tid & 63, wave = __builtin_amdgcn_readfirstlane(tid >> 6);
;     volatile LAS int* box = (volatile LAS int*)(lds + LDS_MISC + 2048);
;     int r = -1; unsigned pollv = 0u;
;     if (tid == 0) { int stop0 = 0; if (cnt) stop0 = (__hip_atomic_load(cnt, __ATOMIC_RELAXED, __HIP_MEMORY_SCOPE_AGENT) >= target) ? 1 : 0;
;         box[0] = stop0 ? -1 : (int)__hip_atomic_fetch_add(tilectr, 1u, __ATOMIC_RELAXED, __HIP_MEMORY_SCOPE_AGENT); box[1] = stop0; }
;     __syncthreads();
;     int idx = box[0], stop = box[1];
;     const int sw = lane & 7;
.LBB0_2405:
	s_or_b64 exec, exec, s[4:5]
	s_add_i32 s9, 0, 0x20800
	v_mov_b32_e32 v1, s9
	s_waitcnt lgkmcnt(0)
	s_barrier
	ds_read_b32 v1, v1
	s_add_i32 s34, 0, 0x20804
	v_mov_b32_e32 v2, s34
	ds_read_b32 v66, v2
	s_movk_i32 s4, 0x29ff
	v_and_b32_e32 v75, 63, v0
	s_waitcnt lgkmcnt(1)
	v_cmp_lt_u32_e32 vcc, s4, v1
	s_mov_b32 s15, 0
	v_readfirstlane_b32 s18, v1
	v_lshlrev_b32_e32 v74, 2, v75
	s_cbranch_vccnz .LBB0_2423
	s_lshr_b32 s6, s14, 6
	v_bitop3_b32 v1, s6, v0, 7 bitop3:0x78
	v_lshlrev_b32_e32 v3, 4, v1
	v_lshrrev_b32_e32 v1, 5, v0
	v_xor_b32_e32 v1, v1, v0
	s_lshl_b32 s35, s6, 4
	v_lshlrev_b32_e32 v1, 4, v1
	v_and_b32_e32 v1, 0x70, v1
	s_add_u32 s38, s36, 0x152c0000
	v_add_u32_e32 v4, 0, v1
	v_lshlrev_b32_e32 v1, 4, v0
	s_addc_u32 s40, s37, 0
	v_and_b32_e32 v76, 0x70, v1
	v_lshrrev_b32_e32 v1, 3, v0
	v_or_b32_e32 v6, 0x200, v0
	v_or_b32_e32 v8, 0x600, v0
	s_add_u32 s16, s36, 0x5cec0000
	v_lshrrev_b32_e32 v82, 3, v6
	v_or_b32_e32 v83, 0x80, v1
	v_lshrrev_b32_e32 v84, 3, v8
	s_addc_u32 s17, s37, 0
	v_lshl_add_u32 v2, v75, 9, 0
	v_mov_b32_e32 v79, 0
	v_lshlrev_b32_e32 v5, 7, v1
	v_lshlrev_b32_e32 v6, 7, v82
	v_lshlrev_b32_e32 v7, 7, v83
	v_lshlrev_b32_e32 v8, 7, v84
	s_add_u32 s41, s36, 0x72c0000
	v_cmp_ne_u32_e64 s[4:5], 0, v0
	v_mov_b32_e32 v77, v79
	s_addc_u32 s42, s37, 0
	v_mov_b32_e32 v96, -1
	s_mov_b32 s43, 0xc3e00000
	s_mov_b32 s44, 0x42fe0000
	s_mov_b32 s45, 0x4b3fff81
	s_mov_b32 s46, 0xc0c0400
	s_mov_b32 s47, 0x5040100
	v_add_u32_e32 v85, v4, v5
	v_add_u32_e32 v86, v4, v6
	v_add_u32_e32 v87, v4, v7
	v_add_u32_e32 v88, v4, v8
	s_movk_i32 s48, 0x2a00
	v_mov_b32_e32 v89, 0x100
	v_mov_b32_e32 v90, 0xf8
	v_mov_b32_e32 v91, 0x3800000
	v_mov_b32_e32 v92, 0x7000
	v_add_u32_e32 v93, v2, v3
	v_mov_b32_e32 v94, 0x43e00000
	v_mov_b32_e32 v95, 0x4b40007f
	v_mov_b64_e32 v[240:241], s[28:29]
	flat_load_dwordx2 v[242:243], v[240:241] offset:256
	flat_load_dwordx2 v[244:245], v[240:241] offset:248
	flat_load_dwordx2 v[240:241], v[240:241] offset:264
	s_waitcnt vmcnt(0) lgkmcnt(0)
	s_branch .LBB0_2408

; __device__ __forceinline__ TD tr_get(const Ctx& P, int it, int lane, int wave) {
;     ...
;     if (r < TR_I8) { const int nn = (r % 448) * 256 + q4, k0 = (r / 448) * 128; const int e = nn / 14336, n = nn % 14336, j = n >> 8, half = (n >> 7) & 1, w = n & 127;
;         t.p = (half ? P.in[32] : P.in[31]) + (size_t)e * DM * DFFE + (size_t)(k0 + kw) * DFFE + j * 128 + w; t.ld = DFFE; t.fp8 = 2; t.cm = (const float*)(ws + WS_MCM) + nn;
;         t.dst = ws + WS_WM1 + (size_t)(nn - q4) * 2048 + k0; t.dpitch = 2048; return t; } r -= TR_I8;
;     { const int nn = (r % 64) * 256 + q4, k0 = (r / 64) * 128; const int e = nn >> 11, n = nn & 2047;
;         t.p = P.in[33] + (size_t)e * DFFE * DM + (size_t)(k0 + kw) * DM + n; t.ld = DM; t.wscale = W2S; t.fp8 = 1;
;         t.dst = ws + WS_WM2 + (size_t)(nn - q4) * DFFE + k0; t.dpitch = DFFE; return t; }
.LBB0_2411:
.LBB0_2412:
	s_bfe_u32 s6, s18, 0xa0006
	s_mulk_i32 s6, 0x2493
	s_lshr_b32 s6, s6, 16
	s_mul_i32 s7, s6, 0x1c0
	s_sub_i32 s7, s18, s7
	s_and_b32 s14, s7, 0xffff
	v_lshl_or_b32 v4, s14, 8, v74
	v_mul_hi_u32_u24_e32 v2, 0x924925, v4
	v_lshrrev_b32_e32 v2, 5, v2
	v_mul_u32_u24_e32 v2, 0x3800, v2
	v_sub_u32_e32 v5, v4, v2
	v_and_b32_e32 v2, 0x80, v5
	v_cmp_eq_u32_e32 vcc, 0, v2
	s_mov_b64 s[18:19], 0x800
	s_bfe_u32 s19, s7, 0xd0003
	v_cndmask_b32_e32 v78, v89, v90, vcc
	v_cndmask_b32_e32 v2, v242, v244, vcc
	v_cndmask_b32_e32 v3, v243, v245, vcc
	s_lshl_b32 s6, s6, 7
	s_mulk_i32 s19, 0x2493
	s_add_i32 s14, s35, s6
	s_lshl_b32 s7, s7, 19
	s_lshr_b32 s19, s19, 16
	s_add_u32 s7, s41, s7
	s_addc_u32 s21, s42, 0
	s_add_u32 s20, s7, s6
	v_and_b32_e32 v6, 0x7c, v5
	v_lshlrev_b32_e32 v5, 1, v5
	v_and_b32_e32 v78, 0x7e00, v5
	s_mov_b32 s49, 1.0
	s_addc_u32 s21, s21, 0
	s_waitcnt lgkmcnt(0)
	v_mad_u64_u32 v[2:3], s[6:7], s19, v91, v[2:3]
	v_mad_u64_u32 v[2:3], s[6:7], s14, v92, v[2:3]
	v_lshl_add_u64 v[2:3], v[2:3], 0, v[78:79]
	v_lshlrev_b32_e32 v78, 2, v6
	v_lshl_add_u64 v[6:7], v[2:3], 0, v[78:79]
	v_lshlrev_b32_e32 v78, 2, v4
	v_lshl_add_u64 v[80:81], s[16:17], 0, v[78:79]
	s_mov_b64 s[6:7], 0x1c00
